# speedup vs baseline: 1.0090x; 1.0010x over previous
.LBB1_11:
	s_waitcnt lgkmcnt(0)
	s_waitcnt lgkmcnt(0)
	s_barrier
	v_add_u32_e32 v110, s3, v1
	v_add_u32_e32 v134, s3, v152
	ds_read_b128 v[98:101], v110
	ds_read_b128 v[102:105], v110 offset:1024
	ds_read_b128 v[106:109], v110 offset:2048
	ds_read_b128 v[110:113], v110 offset:3072
	ds_read_b128 v[114:117], v134 offset:16384
	ds_read_b128 v[118:121], v134 offset:17408
	ds_read_b128 v[122:125], v134 offset:18432
	ds_read_b128 v[126:129], v134 offset:19456
	ds_read_b128 v[130:133], v134 offset:20480
	ds_read_b128 v[134:137], v134 offset:21504
	s_addk_i32 s3, 0x7000
	s_barrier
	s_setprio 1
	s_waitcnt lgkmcnt(5)
	v_mfma_f32_16x16x32_f16 v[94:97], v[114:117], v[98:101], v[94:97]
	s_cmp_lg_u32 s3, 0x23000
	s_cselect_b32 s3, s3, 0
	s_waitcnt lgkmcnt(4)
	v_mfma_f32_16x16x32_f16 v[90:93], v[118:121], v[98:101], v[90:93]
	s_waitcnt lgkmcnt(3)
	v_mfma_f32_16x16x32_f16 v[86:89], v[122:125], v[98:101], v[86:89]
	s_waitcnt lgkmcnt(2)
	v_mfma_f32_16x16x32_f16 v[82:85], v[126:129], v[98:101], v[82:85]
	s_waitcnt lgkmcnt(1)
	v_mfma_f32_16x16x32_f16 v[78:81], v[130:133], v[98:101], v[78:81]
	s_waitcnt lgkmcnt(0)
	v_mfma_f32_16x16x32_f16 v[74:77], v[134:137], v[98:101], v[74:77]
	v_mfma_f32_16x16x32_f16 v[70:73], v[114:117], v[102:105], v[70:73]
	v_mfma_f32_16x16x32_f16 v[66:69], v[118:121], v[102:105], v[66:69]
	v_mfma_f32_16x16x32_f16 v[62:65], v[122:125], v[102:105], v[62:65]
	v_mfma_f32_16x16x32_f16 v[58:61], v[126:129], v[102:105], v[58:61]
	v_mfma_f32_16x16x32_f16 v[54:57], v[130:133], v[102:105], v[54:57]
	v_mfma_f32_16x16x32_f16 v[50:53], v[134:137], v[102:105], v[50:53]
	v_mfma_f32_16x16x32_f16 v[46:49], v[114:117], v[106:109], v[46:49]
	v_mfma_f32_16x16x32_f16 v[42:45], v[118:121], v[106:109], v[42:45]
	v_mfma_f32_16x16x32_f16 v[38:41], v[122:125], v[106:109], v[38:41]
	v_mfma_f32_16x16x32_f16 v[34:37], v[126:129], v[106:109], v[34:37]
	v_mfma_f32_16x16x32_f16 v[30:33], v[130:133], v[106:109], v[30:33]
	v_mfma_f32_16x16x32_f16 v[26:29], v[134:137], v[106:109], v[26:29]
	v_mfma_f32_16x16x32_f16 v[22:25], v[114:117], v[110:113], v[22:25]
	v_mfma_f32_16x16x32_f16 v[18:21], v[118:121], v[110:113], v[18:21]
	v_mfma_f32_16x16x32_f16 v[14:17], v[122:125], v[110:113], v[14:17]
	v_mfma_f32_16x16x32_f16 v[10:13], v[126:129], v[110:113], v[10:13]
	s_waitcnt lgkmcnt(0)
	s_barrier
	v_mfma_f32_16x16x32_f16 v[6:9], v[130:133], v[110:113], v[6:9]
	v_mfma_f32_16x16x32_f16 v[2:5], v[134:137], v[110:113], v[2:5]
	s_setprio 0
	v_add_u32_e32 v110, s3, v1
	v_add_u32_e32 v134, s3, v152
	ds_read_b128 v[98:101], v110
	ds_read_b128 v[102:105], v110 offset:1024
	ds_read_b128 v[106:109], v110 offset:2048
	ds_read_b128 v[110:113], v110 offset:3072
	ds_read_b128 v[114:117], v134 offset:16384
	ds_read_b128 v[118:121], v134 offset:17408
	ds_read_b128 v[122:125], v134 offset:18432
	ds_read_b128 v[126:129], v134 offset:19456
	ds_read_b128 v[130:133], v134 offset:20480
	ds_read_b128 v[134:137], v134 offset:21504
	s_addk_i32 s3, 0x7000
	s_barrier
	s_setprio 1
	s_waitcnt lgkmcnt(5)
	v_mfma_f32_16x16x32_f16 v[94:97], v[114:117], v[98:101], v[94:97]
	s_cmp_lg_u32 s3, 0x23000
	s_cselect_b32 s3, s3, 0
	s_waitcnt lgkmcnt(4)
	v_mfma_f32_16x16x32_f16 v[90:93], v[118:121], v[98:101], v[90:93]
	s_waitcnt lgkmcnt(3)
	v_mfma_f32_16x16x32_f16 v[86:89], v[122:125], v[98:101], v[86:89]
	s_waitcnt lgkmcnt(2)
	v_mfma_f32_16x16x32_f16 v[82:85], v[126:129], v[98:101], v[82:85]
	s_waitcnt lgkmcnt(1)
	v_mfma_f32_16x16x32_f16 v[78:81], v[130:133], v[98:101], v[78:81]
	s_waitcnt lgkmcnt(0)
	v_mfma_f32_16x16x32_f16 v[74:77], v[134:137], v[98:101], v[74:77]
	v_mfma_f32_16x16x32_f16 v[70:73], v[114:117], v[102:105], v[70:73]
	v_mfma_f32_16x16x32_f16 v[66:69], v[118:121], v[102:105], v[66:69]
	v_mfma_f32_16x16x32_f16 v[62:65], v[122:125], v[102:105], v[62:65]
	v_mfma_f32_16x16x32_f16 v[58:61], v[126:129], v[102:105], v[58:61]
	v_mfma_f32_16x16x32_f16 v[54:57], v[130:133], v[102:105], v[54:57]
	v_mfma_f32_16x16x32_f16 v[50:53], v[134:137], v[102:105], v[50:53]
	v_mfma_f32_16x16x32_f16 v[46:49], v[114:117], v[106:109], v[46:49]
	v_mfma_f32_16x16x32_f16 v[42:45], v[118:121], v[106:109], v[42:45]
	v_mfma_f32_16x16x32_f16 v[38:41], v[122:125], v[106:109], v[38:41]
	v_mfma_f32_16x16x32_f16 v[34:37], v[126:129], v[106:109], v[34:37]
	v_mfma_f32_16x16x32_f16 v[30:33], v[130:133], v[106:109], v[30:33]
	v_mfma_f32_16x16x32_f16 v[26:29], v[134:137], v[106:109], v[26:29]
	v_mfma_f32_16x16x32_f16 v[22:25], v[114:117], v[110:113], v[22:25]
	v_mfma_f32_16x16x32_f16 v[18:21], v[118:121], v[110:113], v[18:21]
	v_mfma_f32_16x16x32_f16 v[14:17], v[122:125], v[110:113], v[14:17]
	v_mfma_f32_16x16x32_f16 v[10:13], v[126:129], v[110:113], v[10:13]
	v_mfma_f32_16x16x32_f16 v[6:9], v[130:133], v[110:113], v[6:9]
	v_mfma_f32_16x16x32_f16 v[2:5], v[134:137], v[110:113], v[2:5]
	s_setprio 0
	s_add_i32 s2, s2, -2
	s_cmp_eq_u32 s2, 0
	s_cbranch_scc0 .LBB1_11
	s_waitcnt lgkmcnt(0)
	s_barrier
	s_lshl_b32 s2, s17, 6
	s_or_b32 s2, s2, s18
	s_add_i32 s14, s16, s10
	s_cmpk_lt_i32 s14, 0x400
	s_cselect_b64 vcc, -1, 0
	s_ashr_i32 s12, s14, 10
	v_or_b32_e32 v99, s2, v153
	s_lshr_b32 s2, s2, 7
	s_ashr_i32 s13, s12, 31
	s_and_b32 s15, s2, 0xf0
	s_bfe_u32 s18, s14, 0x40006
	s_lshl_b64 s[12:13], s[12:13], 24
	s_add_u32 s19, s4, s12
	v_mov_b32_e32 v102, s7
	v_mov_b32_e32 v103, s6
	s_addc_u32 s20, s5, s13
	s_or_b32 s12, s15, s18
	v_cndmask_b32_e32 v98, v102, v103, vcc
	v_lshlrev_b32_e32 v99, 6, v99
	s_lshl_b32 s12, s12, 18
	v_lshlrev_b32_e32 v155, 3, v154
	v_mov_b32_e32 v139, 0
	v_and_b32_e32 v142, 0x1f3c0, v99
	v_pk_mul_f32 v[96:97], v[98:99], v[96:97] op_sel_hi:[0,1]
	s_add_u32 s12, s19, s12
	v_pk_mul_f32 v[94:95], v[98:99], v[94:95] op_sel_hi:[0,1]
	v_pk_mul_f32 v[100:101], v[98:99], v[92:93] op_sel_hi:[0,1]
	v_pk_mul_f32 v[90:91], v[98:99], v[90:91] op_sel_hi:[0,1]
	v_cvt_pk_f16_f32 v93, v96, v97
	v_and_or_b32 v144, s16, 32, v155
	s_addc_u32 s13, s20, 0
	v_lshlrev_b32_e32 v96, 1, v142
	v_mov_b32_e32 v97, v139
	s_add_i32 s21, s14, 32
	v_cvt_pk_f16_f32 v92, v94, v95
	v_cvt_pk_f16_f32 v94, v90, v91
	v_cvt_pk_f16_f32 v95, v100, v101
	v_lshl_add_u64 v[100:101], s[12:13], 0, v[96:97]
	v_lshlrev_b32_e32 v90, 1, v144
	v_mov_b32_e32 v91, v139
	s_cmpk_lt_i32 s14, 0x3e0
	v_lshl_add_u64 v[100:101], v[100:101], 0, v[90:91]
	s_cselect_b64 vcc, -1, 0
	s_ashr_i32 s12, s21, 10
	global_store_dwordx4 v[100:101], v[92:95], off sc1
	s_ashr_i32 s13, s12, 31
	s_bfe_u32 s22, s21, 0x40006
	v_cndmask_b32_e32 v92, v102, v103, vcc
	v_pk_mul_f32 v[88:89], v[92:93], v[88:89] op_sel_hi:[0,1]
	v_pk_mul_f32 v[86:87], v[92:93], v[86:87] op_sel_hi:[0,1]
	v_pk_mul_f32 v[84:85], v[92:93], v[84:85] op_sel_hi:[0,1]
	s_lshl_b64 s[12:13], s[12:13], 24
	v_cvt_pk_f16_f32 v86, v86, v87
	v_cvt_pk_f16_f32 v87, v88, v89
	v_cvt_pk_f16_f32 v89, v84, v85
	v_and_or_b32 v84, s21, 32, v155
	s_add_u32 s21, s4, s12
	s_addc_u32 s23, s5, s13
	s_or_b32 s12, s15, s22
	s_lshl_b32 s12, s12, 18
	s_add_u32 s12, s21, s12
	s_addc_u32 s13, s23, 0
	s_add_i32 s24, s14, 64
	v_pk_mul_f32 v[82:83], v[92:93], v[82:83] op_sel_hi:[0,1]
	s_cmpk_lt_i32 s14, 0x3c0
	v_cvt_pk_f16_f32 v88, v82, v83
	v_lshl_add_u64 v[82:83], s[12:13], 0, v[96:97]
	s_cselect_b64 vcc, -1, 0
	s_ashr_i32 s12, s24, 10
	s_ashr_i32 s13, s12, 31
	s_bfe_u32 s24, s24, 0x40006
	s_lshl_b64 s[12:13], s[12:13], 24
	s_add_u32 s25, s4, s12
	v_lshlrev_b32_e32 v84, 1, v84
	v_mov_b32_e32 v85, v139
	s_addc_u32 s26, s5, s13
	s_or_b32 s12, s15, s24
	v_lshl_add_u64 v[82:83], v[82:83], 0, v[84:85]
	s_lshl_b32 s12, s12, 18
	global_store_dwordx4 v[82:83], v[86:89], off sc1
	v_cndmask_b32_e32 v82, v102, v103, vcc
	s_add_u32 s12, s25, s12
	s_mov_b32 s3, 0
	v_pk_mul_f32 v[78:79], v[82:83], v[78:79] op_sel_hi:[0,1]
	s_addc_u32 s13, s26, 0
	s_and_b32 s2, s2, 0xfffff0
	v_pk_mul_f32 v[86:87], v[82:83], v[76:77] op_sel_hi:[0,1]
	v_pk_mul_f32 v[76:77], v[82:83], v[74:75] op_sel_hi:[0,1]
	v_cvt_pk_f16_f32 v74, v78, v79
	v_lshl_add_u64 v[78:79], s[12:13], 0, v[96:97]
	s_or_b32 s12, s2, s18
	s_mov_b32 s13, s3
	v_pk_mul_f32 v[80:81], v[82:83], v[80:81] op_sel_hi:[0,1]
	s_lshl_b64 s[12:13], s[12:13], 18
	v_cvt_pk_f16_f32 v75, v80, v81
	v_cvt_pk_f16_f32 v76, v76, v77
	v_cvt_pk_f16_f32 v77, v86, v87
	v_lshl_add_u64 v[78:79], v[78:79], 0, v[90:91]
	s_add_u32 s12, s19, s12
	v_mov_b32_e32 v138, s15
	global_store_dwordx4 v[78:79], v[74:77], off sc1
	s_mov_b32 s27, 0x1ffc0
	s_addc_u32 s13, s20, s13
	v_mov_b32_e32 v74, 0x400
	s_or_b32 s14, s2, s22
	s_mov_b32 s15, s3
	v_bitop3_b32 v146, v99, s27, v74 bitop3:0xc8
	v_pk_mul_f32 v[70:71], v[98:99], v[70:71] op_sel_hi:[0,1]
	s_lshl_b64 s[14:15], s[14:15], 18
	v_pk_mul_f32 v[72:73], v[98:99], v[72:73] op_sel_hi:[0,1]
	v_pk_mul_f32 v[74:75], v[98:99], v[68:69] op_sel_hi:[0,1]
	v_pk_mul_f32 v[68:69], v[98:99], v[66:67] op_sel_hi:[0,1]
	v_cvt_pk_f16_f32 v66, v70, v71
	v_lshlrev_b32_e32 v70, 1, v146
	v_mov_b32_e32 v71, v139
	s_add_u32 s14, s21, s14
	v_mov_b64_e32 v[140:141], s[2:3]
	v_cvt_pk_f16_f32 v67, v72, v73
	v_lshl_add_u64 v[72:73], s[12:13], 0, v[70:71]
	s_addc_u32 s15, s23, s15
	s_or_b32 s2, s2, s24
	v_cvt_pk_f16_f32 v68, v68, v69
	v_cvt_pk_f16_f32 v69, v74, v75
	v_lshl_add_u64 v[72:73], v[72:73], 0, v[90:91]
	v_pk_mul_f32 v[62:63], v[92:93], v[62:63] op_sel_hi:[0,1]
	s_lshl_b64 s[2:3], s[2:3], 18
	global_store_dwordx4 v[72:73], v[66:69], off sc1
	v_pk_mul_f32 v[64:65], v[92:93], v[64:65] op_sel_hi:[0,1]
	s_add_u32 s2, s25, s2
	v_pk_mul_f32 v[66:67], v[92:93], v[60:61] op_sel_hi:[0,1]
	v_pk_mul_f32 v[60:61], v[92:93], v[58:59] op_sel_hi:[0,1]
	v_cvt_pk_f16_f32 v58, v62, v63
	v_lshl_add_u64 v[62:63], s[14:15], 0, v[70:71]
	v_cvt_pk_f16_f32 v59, v64, v65
	v_cvt_pk_f16_f32 v60, v60, v61
	v_cvt_pk_f16_f32 v61, v66, v67
	v_lshl_add_u64 v[62:63], v[62:63], 0, v[84:85]
	v_pk_mul_f32 v[54:55], v[82:83], v[54:55] op_sel_hi:[0,1]
	s_addc_u32 s3, s26, s3
	global_store_dwordx4 v[62:63], v[58:61], off sc1
	v_pk_mul_f32 v[56:57], v[82:83], v[56:57] op_sel_hi:[0,1]
	v_pk_mul_f32 v[46:47], v[98:99], v[46:47] op_sel_hi:[0,1]
	v_pk_mul_f32 v[58:59], v[82:83], v[52:53] op_sel_hi:[0,1]
	v_pk_mul_f32 v[52:53], v[82:83], v[50:51] op_sel_hi:[0,1]
	v_cvt_pk_f16_f32 v50, v54, v55
	v_lshl_add_u64 v[54:55], s[2:3], 0, v[70:71]
	v_cvt_pk_f16_f32 v51, v56, v57
	v_cvt_pk_f16_f32 v52, v52, v53
	v_cvt_pk_f16_f32 v53, v58, v59
	v_lshl_add_u64 v[54:55], v[54:55], 0, v[90:91]
	global_store_dwordx4 v[54:55], v[50:53], off sc1
	v_pk_mul_f32 v[48:49], v[98:99], v[48:49] op_sel_hi:[0,1]
	v_pk_mul_f32 v[38:39], v[92:93], v[38:39] op_sel_hi:[0,1]
	v_mov_b32_e32 v50, 0x800
	v_bitop3_b32 v148, v99, s27, v50 bitop3:0xc8
	v_pk_mul_f32 v[50:51], v[98:99], v[44:45] op_sel_hi:[0,1]
	v_pk_mul_f32 v[44:45], v[98:99], v[42:43] op_sel_hi:[0,1]
	v_cvt_pk_f16_f32 v42, v46, v47
	v_lshlrev_b32_e32 v46, 1, v148
	v_mov_b32_e32 v47, v139
	v_cvt_pk_f16_f32 v43, v48, v49
	v_lshl_add_u64 v[48:49], s[12:13], 0, v[46:47]
	v_cvt_pk_f16_f32 v44, v44, v45
	v_cvt_pk_f16_f32 v45, v50, v51
	v_lshl_add_u64 v[48:49], v[48:49], 0, v[90:91]
	global_store_dwordx4 v[48:49], v[42:45], off sc1
	v_pk_mul_f32 v[40:41], v[92:93], v[40:41] op_sel_hi:[0,1]
	v_pk_mul_f32 v[30:31], v[82:83], v[30:31] op_sel_hi:[0,1]
	v_pk_mul_f32 v[42:43], v[92:93], v[36:37] op_sel_hi:[0,1]
	v_pk_mul_f32 v[36:37], v[92:93], v[34:35] op_sel_hi:[0,1]
	v_cvt_pk_f16_f32 v34, v38, v39
	v_lshl_add_u64 v[38:39], s[14:15], 0, v[46:47]
	v_cvt_pk_f16_f32 v35, v40, v41
	v_cvt_pk_f16_f32 v36, v36, v37
	v_cvt_pk_f16_f32 v37, v42, v43
	v_lshl_add_u64 v[38:39], v[38:39], 0, v[84:85]
	global_store_dwordx4 v[38:39], v[34:37], off sc1
	v_pk_mul_f32 v[32:33], v[82:83], v[32:33] op_sel_hi:[0,1]
	v_pk_mul_f32 v[22:23], v[98:99], v[22:23] op_sel_hi:[0,1]
	v_pk_mul_f32 v[34:35], v[82:83], v[28:29] op_sel_hi:[0,1]
	v_pk_mul_f32 v[28:29], v[82:83], v[26:27] op_sel_hi:[0,1]
	v_cvt_pk_f16_f32 v26, v30, v31
	v_lshl_add_u64 v[30:31], s[2:3], 0, v[46:47]
	v_cvt_pk_f16_f32 v27, v32, v33
	v_cvt_pk_f16_f32 v28, v28, v29
	v_cvt_pk_f16_f32 v29, v34, v35
	v_lshl_add_u64 v[30:31], v[30:31], 0, v[90:91]
	global_store_dwordx4 v[30:31], v[26:29], off sc1
	v_pk_mul_f32 v[24:25], v[98:99], v[24:25] op_sel_hi:[0,1]
	v_pk_mul_f32 v[14:15], v[92:93], v[14:15] op_sel_hi:[0,1]
	v_mov_b32_e32 v26, 0xc00
	v_bitop3_b32 v150, v99, s27, v26 bitop3:0xc8
	v_pk_mul_f32 v[26:27], v[98:99], v[20:21] op_sel_hi:[0,1]
	v_pk_mul_f32 v[20:21], v[98:99], v[18:19] op_sel_hi:[0,1]
	v_cvt_pk_f16_f32 v18, v22, v23
	v_lshlrev_b32_e32 v22, 1, v150
	v_mov_b32_e32 v23, v139
	v_cvt_pk_f16_f32 v19, v24, v25
	v_lshl_add_u64 v[24:25], s[12:13], 0, v[22:23]
	v_cvt_pk_f16_f32 v20, v20, v21
	v_cvt_pk_f16_f32 v21, v26, v27
	v_lshl_add_u64 v[24:25], v[24:25], 0, v[90:91]
	global_store_dwordx4 v[24:25], v[18:21], off sc1
	v_pk_mul_f32 v[16:17], v[92:93], v[16:17] op_sel_hi:[0,1]
	v_pk_mul_f32 v[6:7], v[82:83], v[6:7] op_sel_hi:[0,1]
	v_pk_mul_f32 v[18:19], v[92:93], v[12:13] op_sel_hi:[0,1]
	v_pk_mul_f32 v[12:13], v[92:93], v[10:11] op_sel_hi:[0,1]
	v_cvt_pk_f16_f32 v10, v14, v15
	v_lshl_add_u64 v[14:15], s[14:15], 0, v[22:23]
	v_cvt_pk_f16_f32 v11, v16, v17
	v_cvt_pk_f16_f32 v12, v12, v13
	v_cvt_pk_f16_f32 v13, v18, v19
	v_lshl_add_u64 v[14:15], v[14:15], 0, v[84:85]
	global_store_dwordx4 v[14:15], v[10:13], off sc1
	v_pk_mul_f32 v[8:9], v[82:83], v[8:9] op_sel_hi:[0,1]
	v_mov_b32_e32 v143, v139
	v_pk_mul_f32 v[10:11], v[82:83], v[4:5] op_sel_hi:[0,1]
	v_pk_mul_f32 v[4:5], v[82:83], v[2:3] op_sel_hi:[0,1]
	v_cvt_pk_f16_f32 v2, v6, v7
	v_lshl_add_u64 v[6:7], s[2:3], 0, v[22:23]
	v_cvt_pk_f16_f32 v3, v8, v9
	v_cvt_pk_f16_f32 v4, v4, v5
	v_cvt_pk_f16_f32 v5, v10, v11
	v_lshl_add_u64 v[6:7], v[6:7], 0, v[90:91]
	s_mov_b32 s17, 32
	v_mov_b32_e32 v145, v139
	v_mov_b32_e32 v147, v139
	v_mov_b32_e32 v149, v139
	v_mov_b32_e32 v151, v139
	global_store_dwordx4 v[6:7], v[2:5], off sc1
	s_mov_b32 s2, 0xe000
	v_mov_b32_e32 v6, v139
	v_mov_b32_e32 v2, v139
	v_mov_b32_e32 v3, v139
	v_mov_b32_e32 v4, v139
	v_mov_b32_e32 v5, v139
	v_mov_b32_e32 v7, v139
	v_mov_b32_e32 v8, v139
	v_mov_b32_e32 v9, v139
	v_mov_b32_e32 v10, v139
	v_mov_b32_e32 v11, v139
	v_mov_b32_e32 v12, v139
	v_mov_b32_e32 v13, v139
	v_mov_b32_e32 v14, v139
	v_mov_b32_e32 v15, v139
	v_mov_b32_e32 v16, v139
	v_mov_b32_e32 v17, v139
	v_mov_b32_e32 v18, v139
	v_mov_b32_e32 v19, v139
	v_mov_b32_e32 v20, v139
	v_mov_b32_e32 v21, v139
	v_mov_b32_e32 v22, v139
	v_mov_b32_e32 v24, v139
	v_mov_b32_e32 v25, v139
	v_mov_b32_e32 v26, v139
	v_mov_b32_e32 v27, v139
	v_mov_b32_e32 v28, v139
	v_mov_b32_e32 v29, v139
	v_mov_b32_e32 v30, v139
	v_mov_b32_e32 v31, v139
	v_mov_b32_e32 v32, v139
	v_mov_b32_e32 v33, v139
	v_mov_b32_e32 v34, v139
	v_mov_b32_e32 v35, v139
	v_mov_b32_e32 v36, v139
	v_mov_b32_e32 v37, v139
	v_mov_b32_e32 v38, v139
	v_mov_b32_e32 v39, v139
	v_mov_b32_e32 v40, v139
	v_mov_b32_e32 v41, v139
	v_mov_b32_e32 v42, v139
	v_mov_b32_e32 v43, v139
	v_mov_b32_e32 v44, v139
	v_mov_b32_e32 v45, v139
	v_mov_b32_e32 v46, v139
	v_mov_b32_e32 v48, v139
	v_mov_b32_e32 v49, v139
	v_mov_b32_e32 v50, v139
	v_mov_b32_e32 v51, v139
	v_mov_b32_e32 v52, v139
	v_mov_b32_e32 v53, v139
	v_mov_b32_e32 v54, v139
	v_mov_b32_e32 v55, v139
	v_mov_b32_e32 v56, v139
	v_mov_b32_e32 v57, v139
	v_mov_b32_e32 v58, v139
	v_mov_b32_e32 v59, v139
	v_mov_b32_e32 v60, v139
	v_mov_b32_e32 v61, v139
	v_mov_b32_e32 v62, v139
	v_mov_b32_e32 v63, v139
	v_mov_b32_e32 v64, v139
	v_mov_b32_e32 v65, v139
	v_mov_b32_e32 v66, v139
	v_mov_b32_e32 v67, v139
	v_mov_b32_e32 v68, v139
	v_mov_b32_e32 v69, v139
	v_mov_b32_e32 v70, v139
	v_mov_b32_e32 v72, v139
	v_mov_b32_e32 v73, v139
	v_mov_b32_e32 v74, v139
	v_mov_b32_e32 v75, v139
	v_mov_b32_e32 v76, v139
	v_mov_b32_e32 v77, v139
	v_mov_b32_e32 v78, v139
	v_mov_b32_e32 v79, v139
	v_mov_b32_e32 v80, v139
	v_mov_b32_e32 v81, v139
	v_mov_b32_e32 v82, v139
	v_mov_b32_e32 v83, v139
	v_mov_b32_e32 v84, v139
	v_mov_b32_e32 v86, v139
	v_mov_b32_e32 v87, v139
	v_mov_b32_e32 v88, v139
	v_mov_b32_e32 v89, v139
	v_mov_b32_e32 v90, v139
	v_mov_b32_e32 v92, v139
	v_mov_b32_e32 v93, v139
	v_mov_b32_e32 v94, v139
	v_mov_b32_e32 v95, v139
	v_mov_b32_e32 v96, v139
	s_branch .Lqkv_w03_afterbar

.Lqkv_w03_afterbar:
	v_add_u32_e32 v110, s2, v1
	v_add_u32_e32 v134, s2, v152
	ds_read_b128 v[98:101], v110
	ds_read_b128 v[102:105], v110 offset:1024
	ds_read_b128 v[106:109], v110 offset:2048
	ds_read_b128 v[110:113], v110 offset:3072
	ds_read_b128 v[114:117], v134 offset:16384
	ds_read_b128 v[118:121], v134 offset:17408
	ds_read_b128 v[122:125], v134 offset:18432
	ds_read_b128 v[126:129], v134 offset:19456
	ds_read_b128 v[130:133], v134 offset:20480
	ds_read_b128 v[134:137], v134 offset:21504
	s_addk_i32 s2, 0x7000
	s_barrier
	s_setprio 1
	s_waitcnt lgkmcnt(5)
	v_mfma_f32_16x16x32_f16 v[94:97], v[114:117], v[98:101], v[94:97]
	s_cmp_lg_u32 s2, 0x23000
	s_cselect_b32 s2, s2, 0
	s_waitcnt lgkmcnt(4)
	v_mfma_f32_16x16x32_f16 v[90:93], v[118:121], v[98:101], v[90:93]
	s_waitcnt lgkmcnt(3)
	v_mfma_f32_16x16x32_f16 v[86:89], v[122:125], v[98:101], v[86:89]
	s_waitcnt lgkmcnt(2)
	v_mfma_f32_16x16x32_f16 v[82:85], v[126:129], v[98:101], v[82:85]
	s_waitcnt lgkmcnt(1)
	v_mfma_f32_16x16x32_f16 v[78:81], v[130:133], v[98:101], v[78:81]
	s_waitcnt lgkmcnt(0)
	v_mfma_f32_16x16x32_f16 v[74:77], v[134:137], v[98:101], v[74:77]
	v_mfma_f32_16x16x32_f16 v[70:73], v[114:117], v[102:105], v[70:73]
	v_mfma_f32_16x16x32_f16 v[66:69], v[118:121], v[102:105], v[66:69]
	v_mfma_f32_16x16x32_f16 v[62:65], v[122:125], v[102:105], v[62:65]
	v_mfma_f32_16x16x32_f16 v[58:61], v[126:129], v[102:105], v[58:61]
	v_mfma_f32_16x16x32_f16 v[54:57], v[130:133], v[102:105], v[54:57]
	v_mfma_f32_16x16x32_f16 v[50:53], v[134:137], v[102:105], v[50:53]
	v_mfma_f32_16x16x32_f16 v[46:49], v[114:117], v[106:109], v[46:49]
	v_mfma_f32_16x16x32_f16 v[42:45], v[118:121], v[106:109], v[42:45]
	v_mfma_f32_16x16x32_f16 v[38:41], v[122:125], v[106:109], v[38:41]
	v_mfma_f32_16x16x32_f16 v[34:37], v[126:129], v[106:109], v[34:37]
	v_mfma_f32_16x16x32_f16 v[30:33], v[130:133], v[106:109], v[30:33]
	v_mfma_f32_16x16x32_f16 v[26:29], v[134:137], v[106:109], v[26:29]
	v_mfma_f32_16x16x32_f16 v[22:25], v[114:117], v[110:113], v[22:25]
	v_mfma_f32_16x16x32_f16 v[18:21], v[118:121], v[110:113], v[18:21]
	v_mfma_f32_16x16x32_f16 v[14:17], v[122:125], v[110:113], v[14:17]
	v_mfma_f32_16x16x32_f16 v[10:13], v[126:129], v[110:113], v[10:13]
	s_waitcnt lgkmcnt(0)
	s_barrier
	v_mfma_f32_16x16x32_f16 v[6:9], v[130:133], v[110:113], v[6:9]
	v_mfma_f32_16x16x32_f16 v[2:5], v[134:137], v[110:113], v[2:5]
	s_setprio 0
	v_add_u32_e32 v110, s2, v1
	v_add_u32_e32 v134, s2, v152
	ds_read_b128 v[98:101], v110
	ds_read_b128 v[102:105], v110 offset:1024
	ds_read_b128 v[106:109], v110 offset:2048
	ds_read_b128 v[110:113], v110 offset:3072
	ds_read_b128 v[114:117], v134 offset:16384
	ds_read_b128 v[118:121], v134 offset:17408
	ds_read_b128 v[122:125], v134 offset:18432
	ds_read_b128 v[126:129], v134 offset:19456
	ds_read_b128 v[130:133], v134 offset:20480
	ds_read_b128 v[134:137], v134 offset:21504
	s_addk_i32 s2, 0x7000
	s_barrier
	s_setprio 1
	s_waitcnt lgkmcnt(5)
	v_mfma_f32_16x16x32_f16 v[94:97], v[114:117], v[98:101], v[94:97]
	s_cmp_lg_u32 s2, 0x23000
	s_cselect_b32 s2, s2, 0
	s_waitcnt lgkmcnt(4)
	v_mfma_f32_16x16x32_f16 v[90:93], v[118:121], v[98:101], v[90:93]
	s_waitcnt lgkmcnt(3)
	v_mfma_f32_16x16x32_f16 v[86:89], v[122:125], v[98:101], v[86:89]
	s_waitcnt lgkmcnt(2)
	v_mfma_f32_16x16x32_f16 v[82:85], v[126:129], v[98:101], v[82:85]
	s_waitcnt lgkmcnt(1)
	v_mfma_f32_16x16x32_f16 v[78:81], v[130:133], v[98:101], v[78:81]
	s_waitcnt lgkmcnt(0)
	v_mfma_f32_16x16x32_f16 v[74:77], v[134:137], v[98:101], v[74:77]
	v_mfma_f32_16x16x32_f16 v[70:73], v[114:117], v[102:105], v[70:73]
	v_mfma_f32_16x16x32_f16 v[66:69], v[118:121], v[102:105], v[66:69]
	v_mfma_f32_16x16x32_f16 v[62:65], v[122:125], v[102:105], v[62:65]
	v_mfma_f32_16x16x32_f16 v[58:61], v[126:129], v[102:105], v[58:61]
	v_mfma_f32_16x16x32_f16 v[54:57], v[130:133], v[102:105], v[54:57]
	v_mfma_f32_16x16x32_f16 v[50:53], v[134:137], v[102:105], v[50:53]
	v_mfma_f32_16x16x32_f16 v[46:49], v[114:117], v[106:109], v[46:49]
	v_mfma_f32_16x16x32_f16 v[42:45], v[118:121], v[106:109], v[42:45]
	v_mfma_f32_16x16x32_f16 v[38:41], v[122:125], v[106:109], v[38:41]
	v_mfma_f32_16x16x32_f16 v[34:37], v[126:129], v[106:109], v[34:37]
	v_mfma_f32_16x16x32_f16 v[30:33], v[130:133], v[106:109], v[30:33]
	v_mfma_f32_16x16x32_f16 v[26:29], v[134:137], v[106:109], v[26:29]
	v_mfma_f32_16x16x32_f16 v[22:25], v[114:117], v[110:113], v[22:25]
	v_mfma_f32_16x16x32_f16 v[18:21], v[118:121], v[110:113], v[18:21]
	v_mfma_f32_16x16x32_f16 v[14:17], v[122:125], v[110:113], v[14:17]
	v_mfma_f32_16x16x32_f16 v[10:13], v[126:129], v[110:113], v[10:13]
	v_mfma_f32_16x16x32_f16 v[6:9], v[130:133], v[110:113], v[6:9]
	v_mfma_f32_16x16x32_f16 v[2:5], v[134:137], v[110:113], v[2:5]
	s_setprio 0
	s_add_i32 s17, s17, -2
	s_cmp_eq_u32 s17, 0
	s_cbranch_scc0 .LBB1_13
